# P1 q,k,v epilogue: x16 storage scale folded into the per-column scales once per unit (128 fewer v_mul per unit and lane; power-of-two scaling, same bits)
# speedup vs baseline: 1.0231x; 1.0028x over previous
.LBB0_181:
	v_mul_f32_e32 v106, 0x41800000, v106
	v_mul_f32_e32 v107, 0x41800000, v107
	v_mul_f32_e32 v108, 0x41800000, v108
	v_mul_f32_e32 v109, 0x41800000, v109
	v_mul_f32_e32 v110, 0x41800000, v110
	v_mul_f32_e32 v111, 0x41800000, v111
	v_mul_f32_e32 v112, 0x41800000, v112
	v_mul_f32_e32 v113, 0x41800000, v113
	v_mul_f32_e32 v114, 0x41800000, v114
	v_mul_f32_e32 v115, 0x41800000, v115
	v_mul_f32_e32 v116, 0x41800000, v116
	v_mul_f32_e32 v117, 0x41800000, v117
	v_mul_f32_e32 v118, 0x41800000, v118
	v_mul_f32_e32 v119, 0x41800000, v119
	v_mul_f32_e32 v120, 0x41800000, v120
	v_mul_f32_e32 v121, 0x41800000, v121
	v_cvt_f32_i32_e32 v143, v143
	v_cvt_f32_i32_e32 v145, v145
	v_cvt_f32_i32_e32 v144, v144
	v_cvt_f32_i32_e32 v142, v142
	v_cvt_f32_i32_e32 v139, v139
	v_cvt_f32_i32_e32 v141, v141
	v_cvt_f32_i32_e32 v140, v140
	v_cvt_f32_i32_e32 v138, v138
	s_waitcnt lgkmcnt(0)
	v_pk_mul_f32 v[190:191], v[116:117], v[188:189] op_sel_hi:[1,0]
	v_pk_mul_f32 v[192:193], v[114:115], v[188:189] op_sel_hi:[1,0]
	v_pk_mul_f32 v[144:145], v[190:191], v[144:145]
	v_pk_mul_f32 v[142:143], v[192:193], v[142:143]
	v_pk_mul_f32 v[190:191], v[120:121], v[188:189] op_sel_hi:[1,0]
	v_pk_mul_f32 v[192:193], v[118:119], v[188:189] op_sel_hi:[1,0]
	v_pk_mul_f32 v[140:141], v[190:191], v[140:141]
	v_pk_mul_f32 v[190:191], v[192:193], v[138:139]
	v_mov_b32_e32 v138, 0
	v_cvt_pk_fp8_f32 v138, v142, v143
	v_mov_b32_e32 v139, 0
	v_cvt_pk_fp8_f32 v139, v190, v191
	v_cvt_f32_i32_e32 v135, v135
	v_cvt_f32_i32_e32 v137, v137
	v_cvt_f32_i32_e32 v136, v136
	v_cvt_f32_i32_e32 v134, v134
	v_cvt_f32_i32_e32 v131, v131
	v_cvt_f32_i32_e32 v133, v133
	v_cvt_f32_i32_e32 v132, v132
	v_cvt_f32_i32_e32 v130, v130
	s_mul_hi_i32 s0, s10, 0x2aaaaaab
	v_cvt_pk_fp8_f32 v138, v144, v145 op_sel:[0,0,1]
	v_cvt_pk_fp8_f32 v139, v140, v141 op_sel:[0,0,1]
	v_pk_mul_f32 v[140:141], v[108:109], v[188:189] op_sel_hi:[1,0]
	v_pk_mul_f32 v[142:143], v[106:107], v[188:189] op_sel_hi:[1,0]
	s_lshr_b32 s1, s0, 31
	s_ashr_i32 s0, s0, 1
	v_pk_mul_f32 v[136:137], v[140:141], v[136:137]
	v_pk_mul_f32 v[134:135], v[142:143], v[134:135]
	v_pk_mul_f32 v[140:141], v[112:113], v[188:189] op_sel_hi:[1,0]
	v_pk_mul_f32 v[142:143], v[110:111], v[188:189] op_sel_hi:[1,0]
	s_add_i32 s0, s0, s1
	v_pk_mul_f32 v[132:133], v[140:141], v[132:133]
	v_pk_mul_f32 v[140:141], v[142:143], v[130:131]
	v_mov_b32_e32 v130, 0
	s_mul_i32 s1, s0, 12
	v_cvt_pk_fp8_f32 v130, v134, v135
	v_mov_b32_e32 v131, 0
	s_sub_i32 s1, s10, s1
	v_cvt_pk_fp8_f32 v131, v140, v141
	s_ashr_i32 s4, s1, 2
	s_lshl_b32 s31, s4, 1
	s_sub_i32 s35, 11, s31
	v_and_b32_e32 v194, 0x7cf, v146
	v_cvt_pk_fp8_f32 v131, v132, v133 op_sel:[0,0,1]
	v_lshlrev_b32_e32 v132, s35, v146
	v_and_b32_e32 v132, 0x7fe, v132
	v_lshrrev_b32_e32 v133, s31, v194
	v_add_u32_e32 v134, v132, v133
	v_or_b32_e32 v132, 16, v194
	v_lshlrev_b32_e32 v133, s35, v132
	v_cvt_f32_i32_e32 v129, v129
	v_cvt_f32_i32_e32 v128, v128
	v_and_b32_e32 v133, 0x7fe, v133
	v_lshrrev_b32_e32 v132, s31, v132
	v_cvt_f32_i32_e32 v123, v123
	v_cvt_f32_i32_e32 v122, v122
	v_cvt_pk_fp8_f32 v130, v136, v137 op_sel:[0,0,1]
	v_add_u32_e32 v135, v133, v132
	v_mov_b32_e32 v132, v189
	v_cvt_f32_i32_e32 v127, v127
	v_cvt_f32_i32_e32 v126, v126
	v_pk_mul_f32 v[136:137], v[120:121], v[132:133] op_sel_hi:[1,0]
	v_pk_mul_f32 v[140:141], v[118:119], v[132:133] op_sel_hi:[1,0]
	v_pk_mul_f32 v[128:129], v[136:137], v[128:129]
	v_pk_mul_f32 v[136:137], v[114:115], v[132:133] op_sel_hi:[1,0]
	v_cvt_f32_i32_e32 v125, v125
	v_cvt_f32_i32_e32 v124, v124
	v_pk_mul_f32 v[122:123], v[136:137], v[122:123]
	v_pk_mul_f32 v[126:127], v[140:141], v[126:127]
	v_mov_b32_e32 v140, 0
	v_mov_b32_e32 v141, 0
	v_cvt_pk_fp8_f32 v140, v122, v123
	v_cvt_pk_fp8_f32 v141, v126, v127
	v_pk_mul_f32 v[126:127], v[116:117], v[132:133] op_sel_hi:[1,0]
	v_pk_mul_f32 v[122:123], v[126:127], v[124:125]
	v_add_u32_e32 v143, 0x80, v146
	v_cvt_pk_fp8_f32 v140, v122, v123 op_sel:[0,0,1]
	v_cvt_pk_fp8_f32 v141, v128, v129 op_sel:[0,0,1]
	v_or_b32_e32 v122, 32, v194
	v_lshlrev_b32_e32 v123, s35, v122
	v_and_b32_e32 v123, 0x7fe, v123
	v_lshrrev_b32_e32 v122, s31, v122
	v_add_u32_e32 v123, v123, v122
	v_or_b32_e32 v122, 48, v194
	v_lshlrev_b32_e32 v124, s35, v122
	v_and_b32_e32 v124, 0x7fe, v124
	v_lshrrev_b32_e32 v122, s31, v122
	v_add_u32_e32 v142, v124, v122
	v_and_b32_e32 v124, 0x7cf, v143
	v_lshlrev_b32_e32 v122, s35, v124
	v_and_b32_e32 v122, 0x7fe, v122
	v_lshrrev_b32_e32 v125, s31, v124
	v_add_u32_e32 v125, v122, v125
	v_or_b32_e32 v122, 16, v124
	s_mul_hi_i32 s10, s0, 0x6000000
	s_mul_i32 s12, s0, 0x6000000
	s_lshl_b32 s0, s1, 22
	v_lshlrev_b32_e32 v126, s35, v122
	s_ashr_i32 s5, s4, 31
	s_and_b32 s1, s0, 0xc00000
	s_ashr_i32 s0, s11, 11
	v_and_b32_e32 v126, 0x7fe, v126
	v_lshrrev_b32_e32 v122, s31, v122
	s_add_u32 s12, s48, s12
	v_cmp_ne_u64_e32 vcc, 0, v[162:163]
	v_add_u32_e32 v126, v126, v122
	s_addc_u32 s13, s49, s10
	v_cndmask_b32_e32 v127, v134, v135, vcc
	v_cndmask_b32_e32 v122, v125, v126, vcc
	v_cmp_eq_u32_e32 vcc, 2, v162
	v_cmp_eq_u32_e64 s[10:11], 3, v162
	s_or_b64 s[14:15], s[10:11], vcc
	s_lshl_b64 s[4:5], s[4:5], 24
	v_cndmask_b32_e64 v127, v127, 0, s[14:15]
	v_lshlrev_b32_e32 v146, 7, v127
	s_add_u32 s4, s12, s4
	v_mov_b32_e32 v127, s0
	s_addc_u32 s5, s13, s5
	v_cndmask_b32_e64 v128, v127, 0, s[14:15]
	s_add_u32 s40, s4, s1
	v_ashrrev_i32_e32 v129, 31, v128
	s_addc_u32 s41, s5, 0
	v_lshlrev_b64 v[128:129], 18, v[128:129]
	v_lshl_add_u64 v[136:137], s[40:41], 0, v[128:129]
	v_lshl_add_u64 v[136:137], v[136:137], 0, v[146:147]
	v_lshl_add_u64 v[136:137], v[136:137], 0, s[20:21]
	v_cvt_f32_i32_e32 v103, v103
	v_cvt_f32_i32_e32 v102, v102
	v_lshl_add_u64 v[136:137], v[136:137], 0, v[160:161]
	v_permlane16_swap_b32_e32 v138, v140
	v_permlane16_swap_b32_e32 v139, v141
	v_lshl_add_u64 v[136:137], v[136:137], 0, v[164:165]
	global_store_dwordx4 v[136:137], v[138:141], off
	v_pk_mul_f32 v[136:137], v[112:113], v[132:133] op_sel_hi:[1,0]
	v_cvt_f32_i32_e32 v105, v105
	v_pk_mul_f32 v[138:139], v[110:111], v[132:133] op_sel_hi:[1,0]
	v_mov_b32_e32 v133, v147
	v_pk_mul_f32 v[102:103], v[138:139], v[102:103]
	v_cvt_f32_i32_e32 v104, v104
	v_cvt_pk_fp8_f32 v133, v102, v103
	v_cvt_f32_i32_e32 v99, v99
	v_cvt_f32_i32_e32 v98, v98
	v_pk_mul_f32 v[104:105], v[136:137], v[104:105]
	v_pk_mul_f32 v[136:137], v[106:107], v[132:133] op_sel_hi:[1,0]
	v_cvt_f32_i32_e32 v101, v101
	v_cvt_f32_i32_e32 v100, v100
	v_pk_mul_f32 v[98:99], v[136:137], v[98:99]
	v_pk_mul_f32 v[102:103], v[108:109], v[132:133] op_sel_hi:[1,0]
	v_mov_b32_e32 v132, v147
	v_cvt_pk_fp8_f32 v132, v98, v99
	v_pk_mul_f32 v[98:99], v[102:103], v[100:101]
	s_add_u32 s4, s40, 0x200000
	v_cvt_pk_fp8_f32 v132, v98, v99 op_sel:[0,0,1]
	s_addc_u32 s5, s41, 0
	v_cvt_pk_fp8_f32 v133, v104, v105 op_sel:[0,0,1]
	v_lshl_add_u64 v[98:99], s[4:5], 0, v[128:129]
	v_lshl_add_u64 v[98:99], v[98:99], 0, v[146:147]
	v_lshl_add_u64 v[98:99], v[98:99], 0, s[20:21]
	v_cvt_f32_i32_e32 v95, v95
	v_cvt_f32_i32_e32 v97, v97
	v_cvt_f32_i32_e32 v96, v96
	v_cvt_f32_i32_e32 v94, v94
	v_lshl_add_u64 v[98:99], v[98:99], 0, v[160:161]
	v_cvt_f32_i32_e32 v91, v91
	v_cvt_f32_i32_e32 v93, v93
	v_cvt_f32_i32_e32 v92, v92
	v_cvt_f32_i32_e32 v90, v90
	v_permlane16_swap_b32_e32 v130, v132
	v_permlane16_swap_b32_e32 v131, v133
	v_lshl_add_u64 v[98:99], v[98:99], 0, v[164:165]
	global_store_dwordx4 v[98:99], v[130:133], off
	v_pk_mul_f32 v[98:99], v[116:117], v[186:187] op_sel_hi:[1,0]
	v_pk_mul_f32 v[100:101], v[114:115], v[186:187] op_sel_hi:[1,0]
	v_pk_mul_f32 v[96:97], v[98:99], v[96:97]
	v_pk_mul_f32 v[94:95], v[100:101], v[94:95]
	v_pk_mul_f32 v[98:99], v[120:121], v[186:187] op_sel_hi:[1,0]
	v_pk_mul_f32 v[100:101], v[118:119], v[186:187] op_sel_hi:[1,0]
	v_pk_mul_f32 v[92:93], v[98:99], v[92:93]
	v_pk_mul_f32 v[98:99], v[100:101], v[90:91]
	v_mov_b32_e32 v90, v147
	v_cvt_pk_fp8_f32 v90, v94, v95
	v_mov_b32_e32 v91, v147
	v_cvt_pk_fp8_f32 v91, v98, v99
	v_cvt_f32_i32_e32 v87, v87
	v_cvt_f32_i32_e32 v89, v89
	v_cvt_f32_i32_e32 v88, v88
	v_cvt_f32_i32_e32 v86, v86
	v_cvt_f32_i32_e32 v79, v79
	v_cvt_f32_i32_e32 v81, v81
	v_cvt_f32_i32_e32 v80, v80
	v_cvt_f32_i32_e32 v78, v78
	v_cvt_pk_fp8_f32 v90, v96, v97 op_sel:[0,0,1]
	v_cvt_pk_fp8_f32 v91, v92, v93 op_sel:[0,0,1]
	v_pk_mul_f32 v[92:93], v[108:109], v[186:187] op_sel_hi:[1,0]
	v_pk_mul_f32 v[94:95], v[106:107], v[186:187] op_sel_hi:[1,0]
	v_pk_mul_f32 v[88:89], v[92:93], v[88:89]
	v_pk_mul_f32 v[86:87], v[94:95], v[86:87]
	v_pk_mul_f32 v[92:93], v[112:113], v[186:187] op_sel_hi:[1,0]
	v_pk_mul_f32 v[94:95], v[110:111], v[186:187] op_sel_hi:[1,0]
	v_pk_mul_f32 v[80:81], v[92:93], v[80:81]
	v_pk_mul_f32 v[92:93], v[94:95], v[78:79]
	v_mov_b32_e32 v78, v147
	v_cvt_pk_fp8_f32 v78, v86, v87
	v_mov_b32_e32 v79, v147
	v_cvt_pk_fp8_f32 v79, v92, v93
	v_cvt_f32_i32_e32 v85, v85
	v_cvt_f32_i32_e32 v84, v84
	v_cvt_pk_fp8_f32 v79, v80, v81 op_sel:[0,0,1]
	v_mov_b32_e32 v80, v187
	v_cvt_pk_fp8_f32 v78, v88, v89 op_sel:[0,0,1]
	v_pk_mul_f32 v[86:87], v[120:121], v[80:81] op_sel_hi:[1,0]
	v_cvt_f32_i32_e32 v75, v75
	v_cvt_f32_i32_e32 v74, v74
	v_cvt_f32_i32_e32 v83, v83
	v_cvt_f32_i32_e32 v82, v82
	v_pk_mul_f32 v[84:85], v[86:87], v[84:85]
	v_pk_mul_f32 v[88:89], v[118:119], v[80:81] op_sel_hi:[1,0]
	v_pk_mul_f32 v[86:87], v[114:115], v[80:81] op_sel_hi:[1,0]
	v_cvt_f32_i32_e32 v77, v77
	v_cvt_f32_i32_e32 v76, v76
	v_pk_mul_f32 v[74:75], v[86:87], v[74:75]
	v_pk_mul_f32 v[82:83], v[88:89], v[82:83]
	v_mov_b32_e32 v92, v147
	v_mov_b32_e32 v93, v147
	v_cvt_pk_fp8_f32 v92, v74, v75
	v_cvt_pk_fp8_f32 v93, v82, v83
	v_pk_mul_f32 v[82:83], v[116:117], v[80:81] op_sel_hi:[1,0]
	v_cndmask_b32_e32 v122, v122, v123, vcc
	v_pk_mul_f32 v[74:75], v[82:83], v[76:77]
	v_cmp_eq_u32_e32 vcc, 1, v166
	v_cvt_pk_fp8_f32 v92, v74, v75 op_sel:[0,0,1]
	v_cndmask_b32_e64 v122, v122, v142, s[10:11]
	v_cvt_pk_fp8_f32 v93, v84, v85 op_sel:[0,0,1]
	v_cndmask_b32_e32 v74, v134, v135, vcc
	v_cmp_eq_u32_e64 s[10:11], 2, v166
	s_ashr_i32 s1, s0, 31
	v_cmp_eq_u32_e64 s[12:13], 3, v166
	v_cndmask_b32_e64 v74, v74, v123, s[10:11]
	s_lshl_b64 s[0:1], s[0:1], 18
	v_cndmask_b32_e64 v74, v74, v142, s[12:13]
	s_add_u32 s42, s40, s0
	v_ashrrev_i32_e32 v75, 31, v74
	s_addc_u32 s43, s41, s1
	v_lshlrev_b64 v[74:75], 7, v[74:75]
	v_cvt_f32_i32_e32 v71, v71
	v_cvt_f32_i32_e32 v70, v70
	v_lshl_add_u64 v[76:77], s[42:43], 0, v[74:75]
	v_lshl_add_u64 v[76:77], v[76:77], 0, s[20:21]
	v_lshl_add_u64 v[76:77], v[76:77], 0, v[160:161]
	v_pk_mul_f32 v[82:83], v[110:111], v[80:81] op_sel_hi:[1,0]
	v_permlane16_swap_b32_e32 v90, v92
	v_permlane16_swap_b32_e32 v91, v93
	v_lshl_add_u64 v[76:77], v[76:77], 0, v[164:165]
	v_pk_mul_f32 v[70:71], v[82:83], v[70:71]
	global_store_dwordx4 v[76:77], v[90:93], off
	v_pk_mul_f32 v[76:77], v[112:113], v[80:81] op_sel_hi:[1,0]
	v_mov_b32_e32 v81, v147
	v_cvt_f32_i32_e32 v73, v73
	v_cvt_f32_i32_e32 v72, v72
	v_cvt_pk_fp8_f32 v81, v70, v71
	v_cvt_f32_i32_e32 v59, v59
	v_cvt_f32_i32_e32 v58, v58
	v_cvt_f32_i32_e32 v61, v61
	v_cvt_f32_i32_e32 v60, v60
	v_pk_mul_f32 v[72:73], v[76:77], v[72:73]
	v_pk_mul_f32 v[76:77], v[106:107], v[80:81] op_sel_hi:[1,0]
	v_cvt_f32_i32_e32 v55, v55
	v_cvt_f32_i32_e32 v57, v57
	v_cvt_f32_i32_e32 v56, v56
	v_cvt_f32_i32_e32 v54, v54
	v_pk_mul_f32 v[58:59], v[76:77], v[58:59]
	v_cvt_f32_i32_e32 v51, v51
	v_cvt_f32_i32_e32 v53, v53
	v_cvt_f32_i32_e32 v52, v52
	v_cvt_f32_i32_e32 v50, v50
	v_pk_mul_f32 v[70:71], v[108:109], v[80:81] op_sel_hi:[1,0]
	v_mov_b32_e32 v80, v147
	v_cvt_pk_fp8_f32 v80, v58, v59
	v_pk_mul_f32 v[58:59], v[70:71], v[60:61]
	v_pk_mul_f32 v[60:61], v[116:117], v[184:185] op_sel_hi:[1,0]
	v_pk_mul_f32 v[70:71], v[114:115], v[184:185] op_sel_hi:[1,0]
	v_pk_mul_f32 v[56:57], v[60:61], v[56:57]
	v_pk_mul_f32 v[54:55], v[70:71], v[54:55]
	v_pk_mul_f32 v[60:61], v[120:121], v[184:185] op_sel_hi:[1,0]
	v_pk_mul_f32 v[70:71], v[118:119], v[184:185] op_sel_hi:[1,0]
	v_pk_mul_f32 v[52:53], v[60:61], v[52:53]
	v_pk_mul_f32 v[60:61], v[70:71], v[50:51]
	v_mov_b32_e32 v50, v147
	v_cvt_pk_fp8_f32 v50, v54, v55
	v_mov_b32_e32 v51, v147
	v_cvt_pk_fp8_f32 v51, v60, v61
	v_cvt_pk_fp8_f32 v50, v56, v57 op_sel:[0,0,1]
	v_cvt_f32_i32_e32 v55, v69
	v_cvt_f32_i32_e32 v54, v68
	v_cvt_pk_fp8_f32 v51, v52, v53 op_sel:[0,0,1]
	v_cvt_f32_i32_e32 v53, v67
	v_cvt_f32_i32_e32 v52, v66
	v_cvt_pk_fp8_f32 v80, v58, v59 op_sel:[0,0,1]
	s_add_u32 s0, s4, s0
	v_cvt_pk_fp8_f32 v81, v72, v73 op_sel:[0,0,1]
	s_addc_u32 s1, s5, s1
	v_pk_mul_f32 v[56:57], v[108:109], v[184:185] op_sel_hi:[1,0]
	v_lshl_add_u64 v[58:59], s[0:1], 0, v[74:75]
	v_pk_mul_f32 v[60:61], v[106:107], v[184:185] op_sel_hi:[1,0]
	v_pk_mul_f32 v[54:55], v[56:57], v[54:55]
	v_cvt_f32_i32_e32 v57, v63
	v_cvt_f32_i32_e32 v56, v62
	v_lshl_add_u64 v[58:59], v[58:59], 0, s[20:21]
	v_pk_mul_f32 v[52:53], v[60:61], v[52:53]
	v_cvt_f32_i32_e32 v61, v65
	v_cvt_f32_i32_e32 v60, v64
	v_lshl_add_u64 v[58:59], v[58:59], 0, v[160:161]
	v_permlane16_swap_b32_e32 v78, v80
	v_permlane16_swap_b32_e32 v79, v81
	v_lshl_add_u64 v[58:59], v[58:59], 0, v[164:165]
	v_pk_mul_f32 v[64:65], v[110:111], v[184:185] op_sel_hi:[1,0]
	global_store_dwordx4 v[58:59], v[78:81], off
	v_pk_mul_f32 v[62:63], v[112:113], v[184:185] op_sel_hi:[1,0]
	v_pk_mul_f32 v[56:57], v[64:65], v[56:57]
	v_mov_b32_e32 v59, v54
	v_mov_b32_e32 v54, v147
	v_pk_mul_f32 v[60:61], v[62:63], v[60:61]
	v_mov_b32_e32 v62, v55
	v_cvt_pk_fp8_f32 v54, v52, v53
	v_mov_b32_e32 v55, v147
	v_cvt_f32_i32_e32 v39, v39
	v_cvt_f32_i32_e32 v38, v38
	v_cvt_pk_fp8_f32 v55, v56, v57
	v_cvt_f32_i32_e32 v35, v35
	v_cvt_f32_i32_e32 v34, v34
	v_mov_b32_e32 v56, v185
	v_cvt_f32_i32_e32 v41, v41
	v_cvt_f32_i32_e32 v40, v40
	v_mov_b32_e32 v52, v60
	v_mov_b32_e32 v53, v61
	v_pk_mul_f32 v[60:61], v[118:119], v[56:57] op_sel_hi:[1,0]
	v_cvt_pk_fp8_f32 v55, v52, v53 op_sel:[0,0,1]
	v_pk_mul_f32 v[38:39], v[60:61], v[38:39]
	v_pk_mul_f32 v[60:61], v[114:115], v[56:57] op_sel_hi:[1,0]
	v_pk_mul_f32 v[52:53], v[120:121], v[56:57] op_sel_hi:[1,0]
	v_cvt_f32_i32_e32 v37, v37
	v_cvt_f32_i32_e32 v36, v36
	v_pk_mul_f32 v[34:35], v[60:61], v[34:35]
	v_pk_mul_f32 v[40:41], v[52:53], v[40:41]
	v_mov_b32_e32 v52, v147
	v_mov_b32_e32 v53, v147
	v_cvt_pk_fp8_f32 v52, v34, v35
	v_cvt_pk_fp8_f32 v53, v38, v39
	v_pk_mul_f32 v[38:39], v[116:117], v[56:57] op_sel_hi:[1,0]
	v_ashrrev_i32_e32 v58, 11, v143
	v_pk_mul_f32 v[34:35], v[38:39], v[36:37]
	v_cvt_pk_fp8_f32 v52, v34, v35 op_sel:[0,0,1]
	v_cvt_pk_fp8_f32 v53, v40, v41 op_sel:[0,0,1]
	v_cndmask_b32_e64 v34, v58, v127, s[14:15]
	v_ashrrev_i32_e32 v35, 31, v34
	v_lshlrev_b64 v[34:35], 18, v[34:35]
	v_ashrrev_i32_e32 v123, 31, v122
	v_lshl_add_u64 v[36:37], s[40:41], 0, v[34:35]
	v_lshlrev_b64 v[38:39], 7, v[122:123]
	v_lshl_add_u64 v[36:37], v[36:37], 0, v[38:39]
	v_lshl_add_u64 v[36:37], v[36:37], 0, s[20:21]
	v_cvt_f32_i32_e32 v41, v47
	v_cvt_f32_i32_e32 v40, v46
	v_lshl_add_u64 v[36:37], v[36:37], 0, v[160:161]
	v_permlane16_swap_b32_e32 v50, v52
	v_permlane16_swap_b32_e32 v51, v53
	v_lshl_add_u64 v[36:37], v[36:37], 0, v[164:165]
	global_store_dwordx4 v[36:37], v[50:53], off
	v_cvt_f32_i32_e32 v37, v49
	v_cvt_f32_i32_e32 v36, v48
	v_pk_mul_f32 v[48:49], v[110:111], v[56:57] op_sel_hi:[1,0]
	v_pk_mul_f32 v[46:47], v[112:113], v[56:57] op_sel_hi:[1,0]
	v_pk_mul_f32 v[40:41], v[48:49], v[40:41]
	v_mov_b32_e32 v57, v147
	v_cvt_pk_fp8_f32 v57, v40, v41
	v_cvt_f32_i32_e32 v43, v43
	v_cvt_f32_i32_e32 v42, v42
	v_pk_mul_f32 v[36:37], v[46:47], v[36:37]
	v_pk_mul_f32 v[46:47], v[106:107], v[56:57] op_sel_hi:[1,0]
	v_cvt_f32_i32_e32 v45, v45
	v_cvt_f32_i32_e32 v44, v44
	v_pk_mul_f32 v[42:43], v[46:47], v[42:43]
	v_pk_mul_f32 v[40:41], v[108:109], v[56:57] op_sel_hi:[1,0]
	v_mov_b32_e32 v56, v147
	v_cvt_pk_fp8_f32 v56, v42, v43
	v_pk_mul_f32 v[40:41], v[40:41], v[44:45]
	v_cvt_pk_fp8_f32 v54, v59, v62 op_sel:[0,0,1]
	v_cvt_pk_fp8_f32 v56, v40, v41 op_sel:[0,0,1]
	v_cvt_pk_fp8_f32 v57, v36, v37 op_sel:[0,0,1]
	v_lshl_add_u64 v[34:35], s[4:5], 0, v[34:35]
	v_lshl_add_u64 v[34:35], v[34:35], 0, v[38:39]
	v_lshl_add_u64 v[34:35], v[34:35], 0, s[20:21]
	v_lshl_add_u64 v[34:35], v[34:35], 0, v[160:161]
	v_permlane16_swap_b32_e32 v54, v56
	v_permlane16_swap_b32_e32 v55, v57
	v_lshl_add_u64 v[34:35], v[34:35], 0, v[164:165]
	global_store_dwordx4 v[34:35], v[54:57], off
	v_or_b32_e32 v34, 32, v124
	v_cvt_f32_i32_e32 v23, v23
	v_cvt_f32_i32_e32 v25, v25
	v_cvt_f32_i32_e32 v24, v24
	v_cvt_f32_i32_e32 v22, v22
	v_lshlrev_b32_e32 v35, s35, v34
	v_cvt_f32_i32_e32 v19, v19
	v_cvt_f32_i32_e32 v21, v21
	v_cvt_f32_i32_e32 v20, v20
	v_cvt_f32_i32_e32 v18, v18
	v_and_b32_e32 v35, 0x7fe, v35
	v_lshrrev_b32_e32 v34, s31, v34
	v_add_u32_e32 v38, v35, v34
	v_pk_mul_f32 v[34:35], v[116:117], v[182:183] op_sel_hi:[1,0]
	v_pk_mul_f32 v[36:37], v[114:115], v[182:183] op_sel_hi:[1,0]
	v_pk_mul_f32 v[24:25], v[34:35], v[24:25]
	v_pk_mul_f32 v[22:23], v[36:37], v[22:23]
	v_pk_mul_f32 v[34:35], v[120:121], v[182:183] op_sel_hi:[1,0]
	v_pk_mul_f32 v[36:37], v[118:119], v[182:183] op_sel_hi:[1,0]
	v_pk_mul_f32 v[20:21], v[34:35], v[20:21]
	v_pk_mul_f32 v[34:35], v[36:37], v[18:19]
	v_mov_b32_e32 v18, v147
	v_cvt_pk_fp8_f32 v18, v22, v23
	v_mov_b32_e32 v19, v147
	v_cvt_pk_fp8_f32 v19, v34, v35
	v_cvt_pk_fp8_f32 v18, v24, v25 op_sel:[0,0,1]
	v_cvt_f32_i32_e32 v23, v33
	v_cvt_f32_i32_e32 v22, v32
	v_cvt_pk_fp8_f32 v19, v20, v21 op_sel:[0,0,1]
	v_cvt_f32_i32_e32 v21, v31
	v_cvt_f32_i32_e32 v20, v30
	v_pk_mul_f32 v[24:25], v[108:109], v[182:183] op_sel_hi:[1,0]
	v_cvt_f32_i32_e32 v29, v29
	v_pk_mul_f32 v[22:23], v[24:25], v[22:23]
	v_cvt_f32_i32_e32 v25, v27
	v_cvt_f32_i32_e32 v28, v28
	v_cvt_f32_i32_e32 v24, v26
	v_pk_mul_f32 v[30:31], v[106:107], v[182:183] op_sel_hi:[1,0]
	v_pk_mul_f32 v[26:27], v[112:113], v[182:183] op_sel_hi:[1,0]
	v_pk_mul_f32 v[20:21], v[30:31], v[20:21]
	v_pk_mul_f32 v[30:31], v[110:111], v[182:183] op_sel_hi:[1,0]
	v_pk_mul_f32 v[26:27], v[26:27], v[28:29]
	v_pk_mul_f32 v[24:25], v[30:31], v[24:25]
	v_mov_b32_e32 v28, v22
	v_mov_b32_e32 v22, v147
	v_mov_b32_e32 v29, v23
	v_cvt_pk_fp8_f32 v22, v20, v21
	v_mov_b32_e32 v23, v147
	v_cvt_pk_fp8_f32 v23, v24, v25
	v_cvt_f32_i32_e32 v7, v7
	v_cvt_pk_fp8_f32 v23, v26, v27 op_sel:[0,0,1]
	v_or_b32_e32 v20, 48, v124
	v_lshlrev_b32_e32 v21, s35, v20
	v_cvt_f32_i32_e32 v6, v6
	v_and_b32_e32 v21, 0x7fe, v21
	v_lshrrev_b32_e32 v20, s31, v20
	v_cvt_f32_i32_e32 v3, v3
	v_cvt_f32_i32_e32 v2, v2
	v_add_u32_e32 v25, v21, v20
	v_mov_b32_e32 v24, v183
	v_cvt_f32_i32_e32 v9, v9
	v_cvt_f32_i32_e32 v8, v8
	v_pk_mul_f32 v[26:27], v[118:119], v[24:25] op_sel_hi:[1,0]
	v_pk_mul_f32 v[20:21], v[120:121], v[24:25] op_sel_hi:[1,0]
	v_pk_mul_f32 v[6:7], v[26:27], v[6:7]
	v_pk_mul_f32 v[26:27], v[114:115], v[24:25] op_sel_hi:[1,0]
	v_cvt_f32_i32_e32 v5, v5
	v_cvt_f32_i32_e32 v4, v4
	v_pk_mul_f32 v[2:3], v[26:27], v[2:3]
	v_pk_mul_f32 v[8:9], v[20:21], v[8:9]
	v_mov_b32_e32 v20, v147
	v_mov_b32_e32 v21, v147
	v_cvt_pk_fp8_f32 v20, v2, v3
	v_cvt_pk_fp8_f32 v21, v6, v7
	v_pk_mul_f32 v[6:7], v[116:117], v[24:25] op_sel_hi:[1,0]
	v_pk_mul_f32 v[2:3], v[6:7], v[4:5]
	v_cndmask_b32_e32 v6, v125, v126, vcc
	v_cndmask_b32_e64 v6, v6, v38, s[10:11]
	v_cvt_pk_fp8_f32 v20, v2, v3 op_sel:[0,0,1]
	v_ashrrev_i32_e32 v59, 31, v58
	v_cndmask_b32_e64 v6, v6, v25, s[12:13]
	v_cvt_pk_fp8_f32 v21, v8, v9 op_sel:[0,0,1]
	v_lshlrev_b64 v[2:3], 18, v[58:59]
	v_ashrrev_i32_e32 v7, 31, v6
	v_lshl_add_u64 v[4:5], s[40:41], 0, v[2:3]
	v_lshlrev_b64 v[6:7], 7, v[6:7]
	v_lshl_add_u64 v[4:5], v[4:5], 0, v[6:7]
	v_lshl_add_u64 v[4:5], v[4:5], 0, s[20:21]
	v_cvt_f32_i32_e32 v9, v15
	v_cvt_f32_i32_e32 v8, v14
	v_lshl_add_u64 v[4:5], v[4:5], 0, v[160:161]
	v_permlane16_swap_b32_e32 v18, v20
	v_permlane16_swap_b32_e32 v19, v21
	v_lshl_add_u64 v[4:5], v[4:5], 0, v[164:165]
	global_store_dwordx4 v[4:5], v[18:21], off
	v_cvt_f32_i32_e32 v5, v17
	v_cvt_f32_i32_e32 v4, v16
	v_pk_mul_f32 v[16:17], v[110:111], v[24:25] op_sel_hi:[1,0]
	v_pk_mul_f32 v[14:15], v[112:113], v[24:25] op_sel_hi:[1,0]
	v_pk_mul_f32 v[8:9], v[16:17], v[8:9]
	v_mov_b32_e32 v25, v147
	v_cvt_pk_fp8_f32 v25, v8, v9
	v_cvt_f32_i32_e32 v11, v11
	v_cvt_f32_i32_e32 v10, v10
	v_pk_mul_f32 v[4:5], v[14:15], v[4:5]
	v_pk_mul_f32 v[14:15], v[106:107], v[24:25] op_sel_hi:[1,0]
	v_cvt_f32_i32_e32 v13, v13
	v_cvt_f32_i32_e32 v12, v12
	v_pk_mul_f32 v[10:11], v[14:15], v[10:11]
	v_pk_mul_f32 v[8:9], v[108:109], v[24:25] op_sel_hi:[1,0]
	v_mov_b32_e32 v24, v147
	v_cvt_pk_fp8_f32 v24, v10, v11
	v_pk_mul_f32 v[8:9], v[8:9], v[12:13]
	v_cvt_pk_fp8_f32 v22, v28, v29 op_sel:[0,0,1]
	v_cvt_pk_fp8_f32 v24, v8, v9 op_sel:[0,0,1]
	v_cvt_pk_fp8_f32 v25, v4, v5 op_sel:[0,0,1]
	v_lshl_add_u64 v[2:3], s[4:5], 0, v[2:3]
	v_lshl_add_u64 v[2:3], v[2:3], 0, v[6:7]
	v_lshl_add_u64 v[2:3], v[2:3], 0, s[20:21]
	v_lshl_add_u64 v[2:3], v[2:3], 0, v[160:161]
	v_permlane16_swap_b32_e32 v22, v24
	v_permlane16_swap_b32_e32 v23, v25
	v_lshl_add_u64 v[2:3], v[2:3], 0, v[164:165]
	global_store_dwordx4 v[2:3], v[22:25], off
	s_and_b64 vcc, exec, s[8:9]
	s_mov_b64 s[0:1], -1
	s_cbranch_vccnz .LBB0_152

.LBB0_263:
	v_mul_f32_e32 v106, 0x41800000, v106
	v_mul_f32_e32 v107, 0x41800000, v107
	v_mul_f32_e32 v108, 0x41800000, v108
	v_mul_f32_e32 v109, 0x41800000, v109
	v_mul_f32_e32 v110, 0x41800000, v110
	v_mul_f32_e32 v111, 0x41800000, v111
	v_mul_f32_e32 v112, 0x41800000, v112
	v_mul_f32_e32 v113, 0x41800000, v113
	v_mul_f32_e32 v114, 0x41800000, v114
	v_mul_f32_e32 v115, 0x41800000, v115
	v_mul_f32_e32 v116, 0x41800000, v116
	v_mul_f32_e32 v117, 0x41800000, v117
	v_mul_f32_e32 v118, 0x41800000, v118
	v_mul_f32_e32 v119, 0x41800000, v119
	v_mul_f32_e32 v120, 0x41800000, v120
	v_mul_f32_e32 v121, 0x41800000, v121
	v_cvt_f32_i32_e32 v143, v143
	v_cvt_f32_i32_e32 v145, v145
	v_cvt_f32_i32_e32 v144, v144
	v_cvt_f32_i32_e32 v142, v142
	v_cvt_f32_i32_e32 v139, v139
	v_cvt_f32_i32_e32 v141, v141
	v_cvt_f32_i32_e32 v140, v140
	v_cvt_f32_i32_e32 v138, v138
	s_waitcnt lgkmcnt(0)
	v_pk_mul_f32 v[190:191], v[116:117], v[188:189] op_sel_hi:[1,0]
	v_pk_mul_f32 v[192:193], v[114:115], v[188:189] op_sel_hi:[1,0]
	v_pk_mul_f32 v[144:145], v[190:191], v[144:145]
	v_pk_mul_f32 v[142:143], v[192:193], v[142:143]
	v_pk_mul_f32 v[190:191], v[120:121], v[188:189] op_sel_hi:[1,0]
	v_pk_mul_f32 v[192:193], v[118:119], v[188:189] op_sel_hi:[1,0]
	v_pk_mul_f32 v[140:141], v[190:191], v[140:141]
	v_pk_mul_f32 v[190:191], v[192:193], v[138:139]
	v_mov_b32_e32 v138, 0
	v_cvt_pk_fp8_f32 v138, v142, v143
	v_mov_b32_e32 v139, 0
	v_cvt_pk_fp8_f32 v139, v190, v191
	v_cvt_f32_i32_e32 v135, v135
	v_cvt_f32_i32_e32 v137, v137
	v_cvt_f32_i32_e32 v136, v136
	v_cvt_f32_i32_e32 v134, v134
	v_cvt_f32_i32_e32 v131, v131
	v_cvt_f32_i32_e32 v133, v133
	v_cvt_f32_i32_e32 v132, v132
	v_cvt_f32_i32_e32 v130, v130
	s_mul_hi_i32 s0, s10, 0x2aaaaaab
	v_cvt_pk_fp8_f32 v138, v144, v145 op_sel:[0,0,1]
	v_cvt_pk_fp8_f32 v139, v140, v141 op_sel:[0,0,1]
	v_pk_mul_f32 v[140:141], v[108:109], v[188:189] op_sel_hi:[1,0]
	v_pk_mul_f32 v[142:143], v[106:107], v[188:189] op_sel_hi:[1,0]
	s_lshr_b32 s1, s0, 31
	s_ashr_i32 s0, s0, 1
	v_pk_mul_f32 v[136:137], v[140:141], v[136:137]
	v_pk_mul_f32 v[134:135], v[142:143], v[134:135]
	v_pk_mul_f32 v[140:141], v[112:113], v[188:189] op_sel_hi:[1,0]
	v_pk_mul_f32 v[142:143], v[110:111], v[188:189] op_sel_hi:[1,0]
	s_add_i32 s0, s0, s1
	v_pk_mul_f32 v[132:133], v[140:141], v[132:133]
	v_pk_mul_f32 v[140:141], v[142:143], v[130:131]
	v_mov_b32_e32 v130, 0
	s_mul_i32 s1, s0, 12
	v_cvt_pk_fp8_f32 v130, v134, v135
	v_mov_b32_e32 v131, 0
	s_sub_i32 s1, s10, s1
	v_cvt_pk_fp8_f32 v131, v140, v141
	s_ashr_i32 s4, s1, 2
	s_lshl_b32 s19, s4, 1
	s_sub_i32 s29, 11, s19
	v_and_b32_e32 v194, 0x7cf, v146
	v_cvt_pk_fp8_f32 v131, v132, v133 op_sel:[0,0,1]
	v_lshlrev_b32_e32 v132, s29, v146
	v_and_b32_e32 v132, 0x7fe, v132
	v_lshrrev_b32_e32 v133, s19, v194
	v_add_u32_e32 v134, v132, v133
	v_or_b32_e32 v132, 16, v194
	v_lshlrev_b32_e32 v133, s29, v132
	v_cvt_f32_i32_e32 v129, v129
	v_cvt_f32_i32_e32 v128, v128
	v_and_b32_e32 v133, 0x7fe, v133
	v_lshrrev_b32_e32 v132, s19, v132
	v_cvt_f32_i32_e32 v123, v123
	v_cvt_f32_i32_e32 v122, v122
	v_cvt_pk_fp8_f32 v130, v136, v137 op_sel:[0,0,1]
	v_add_u32_e32 v135, v133, v132
	v_mov_b32_e32 v132, v189
	v_cvt_f32_i32_e32 v127, v127
	v_cvt_f32_i32_e32 v126, v126
	v_pk_mul_f32 v[136:137], v[120:121], v[132:133] op_sel_hi:[1,0]
	v_pk_mul_f32 v[140:141], v[118:119], v[132:133] op_sel_hi:[1,0]
	v_pk_mul_f32 v[128:129], v[136:137], v[128:129]
	v_pk_mul_f32 v[136:137], v[114:115], v[132:133] op_sel_hi:[1,0]
	v_cvt_f32_i32_e32 v125, v125
	v_cvt_f32_i32_e32 v124, v124
	v_pk_mul_f32 v[122:123], v[136:137], v[122:123]
	v_pk_mul_f32 v[126:127], v[140:141], v[126:127]
	v_mov_b32_e32 v140, 0
	v_mov_b32_e32 v141, 0
	v_cvt_pk_fp8_f32 v140, v122, v123
	v_cvt_pk_fp8_f32 v141, v126, v127
	v_pk_mul_f32 v[126:127], v[116:117], v[132:133] op_sel_hi:[1,0]
	v_pk_mul_f32 v[122:123], v[126:127], v[124:125]
	v_add_u32_e32 v143, 0x80, v146
	v_cvt_pk_fp8_f32 v140, v122, v123 op_sel:[0,0,1]
	v_cvt_pk_fp8_f32 v141, v128, v129 op_sel:[0,0,1]
	v_or_b32_e32 v122, 32, v194
	v_lshlrev_b32_e32 v123, s29, v122
	v_and_b32_e32 v123, 0x7fe, v123
	v_lshrrev_b32_e32 v122, s19, v122
	v_add_u32_e32 v123, v123, v122
	v_or_b32_e32 v122, 48, v194
	v_lshlrev_b32_e32 v124, s29, v122
	v_and_b32_e32 v124, 0x7fe, v124
	v_lshrrev_b32_e32 v122, s19, v122
	v_add_u32_e32 v142, v124, v122
	v_and_b32_e32 v124, 0x7cf, v143
	v_lshlrev_b32_e32 v122, s29, v124
	v_and_b32_e32 v122, 0x7fe, v122
	v_lshrrev_b32_e32 v125, s19, v124
	v_add_u32_e32 v125, v122, v125
	v_or_b32_e32 v122, 16, v124
	s_mul_hi_i32 s10, s0, 0x6000000
	s_mul_i32 s12, s0, 0x6000000
	s_lshl_b32 s0, s1, 22
	v_lshlrev_b32_e32 v126, s29, v122
	s_ashr_i32 s5, s4, 31
	s_and_b32 s1, s0, 0xc00000
	s_ashr_i32 s0, s11, 11
	v_and_b32_e32 v126, 0x7fe, v126
	v_lshrrev_b32_e32 v122, s19, v122
	s_add_u32 s12, s48, s12
	v_cmp_ne_u64_e32 vcc, 0, v[162:163]
	v_add_u32_e32 v126, v126, v122
	s_addc_u32 s13, s49, s10
	v_cndmask_b32_e32 v127, v134, v135, vcc
	v_cndmask_b32_e32 v122, v125, v126, vcc
	v_cmp_eq_u32_e32 vcc, 2, v162
	v_cmp_eq_u32_e64 s[10:11], 3, v162
	s_or_b64 s[14:15], s[10:11], vcc
	s_lshl_b64 s[4:5], s[4:5], 24
	v_cndmask_b32_e64 v127, v127, 0, s[14:15]
	v_lshlrev_b32_e32 v146, 7, v127
	s_add_u32 s4, s12, s4
	v_mov_b32_e32 v127, s0
	s_addc_u32 s5, s13, s5
	v_cndmask_b32_e64 v128, v127, 0, s[14:15]
	s_add_u32 s36, s4, s1
	v_ashrrev_i32_e32 v129, 31, v128
	s_addc_u32 s37, s5, 0
	v_lshlrev_b64 v[128:129], 18, v[128:129]
	v_lshl_add_u64 v[136:137], s[36:37], 0, v[128:129]
	v_lshl_add_u64 v[136:137], v[136:137], 0, v[146:147]
	v_lshl_add_u64 v[136:137], v[136:137], 0, s[20:21]
	v_cvt_f32_i32_e32 v103, v103
	v_cvt_f32_i32_e32 v102, v102
	v_lshl_add_u64 v[136:137], v[136:137], 0, v[160:161]
	v_permlane16_swap_b32_e32 v138, v140
	v_permlane16_swap_b32_e32 v139, v141
	v_lshl_add_u64 v[136:137], v[136:137], 0, v[164:165]
	global_store_dwordx4 v[136:137], v[138:141], off
	v_pk_mul_f32 v[136:137], v[112:113], v[132:133] op_sel_hi:[1,0]
	v_cvt_f32_i32_e32 v105, v105
	v_pk_mul_f32 v[138:139], v[110:111], v[132:133] op_sel_hi:[1,0]
	v_mov_b32_e32 v133, v147
	v_pk_mul_f32 v[102:103], v[138:139], v[102:103]
	v_cvt_f32_i32_e32 v104, v104
	v_cvt_pk_fp8_f32 v133, v102, v103
	v_cvt_f32_i32_e32 v99, v99
	v_cvt_f32_i32_e32 v98, v98
	v_pk_mul_f32 v[104:105], v[136:137], v[104:105]
	v_pk_mul_f32 v[136:137], v[106:107], v[132:133] op_sel_hi:[1,0]
	v_cvt_f32_i32_e32 v101, v101
	v_cvt_f32_i32_e32 v100, v100
	v_pk_mul_f32 v[98:99], v[136:137], v[98:99]
	v_pk_mul_f32 v[102:103], v[108:109], v[132:133] op_sel_hi:[1,0]
	v_mov_b32_e32 v132, v147
	v_cvt_pk_fp8_f32 v132, v98, v99
	v_pk_mul_f32 v[98:99], v[102:103], v[100:101]
	s_add_u32 s4, s36, 0x200000
	v_cvt_pk_fp8_f32 v132, v98, v99 op_sel:[0,0,1]
	s_addc_u32 s5, s37, 0
	v_cvt_pk_fp8_f32 v133, v104, v105 op_sel:[0,0,1]
	v_lshl_add_u64 v[98:99], s[4:5], 0, v[128:129]
	v_lshl_add_u64 v[98:99], v[98:99], 0, v[146:147]
	v_lshl_add_u64 v[98:99], v[98:99], 0, s[20:21]
	v_cvt_f32_i32_e32 v95, v95
	v_cvt_f32_i32_e32 v97, v97
	v_cvt_f32_i32_e32 v96, v96
	v_cvt_f32_i32_e32 v94, v94
	v_lshl_add_u64 v[98:99], v[98:99], 0, v[160:161]
	v_cvt_f32_i32_e32 v91, v91
	v_cvt_f32_i32_e32 v93, v93
	v_cvt_f32_i32_e32 v92, v92
	v_cvt_f32_i32_e32 v90, v90
	v_permlane16_swap_b32_e32 v130, v132
	v_permlane16_swap_b32_e32 v131, v133
	v_lshl_add_u64 v[98:99], v[98:99], 0, v[164:165]
	global_store_dwordx4 v[98:99], v[130:133], off
	v_pk_mul_f32 v[98:99], v[116:117], v[186:187] op_sel_hi:[1,0]
	v_pk_mul_f32 v[100:101], v[114:115], v[186:187] op_sel_hi:[1,0]
	v_pk_mul_f32 v[96:97], v[98:99], v[96:97]
	v_pk_mul_f32 v[94:95], v[100:101], v[94:95]
	v_pk_mul_f32 v[98:99], v[120:121], v[186:187] op_sel_hi:[1,0]
	v_pk_mul_f32 v[100:101], v[118:119], v[186:187] op_sel_hi:[1,0]
	v_pk_mul_f32 v[92:93], v[98:99], v[92:93]
	v_pk_mul_f32 v[98:99], v[100:101], v[90:91]
	v_mov_b32_e32 v90, v147
	v_cvt_pk_fp8_f32 v90, v94, v95
	v_mov_b32_e32 v91, v147
	v_cvt_pk_fp8_f32 v91, v98, v99
	v_cvt_f32_i32_e32 v87, v87
	v_cvt_f32_i32_e32 v89, v89
	v_cvt_f32_i32_e32 v88, v88
	v_cvt_f32_i32_e32 v86, v86
	v_cvt_f32_i32_e32 v79, v79
	v_cvt_f32_i32_e32 v81, v81
	v_cvt_f32_i32_e32 v80, v80
	v_cvt_f32_i32_e32 v78, v78
	v_cvt_pk_fp8_f32 v90, v96, v97 op_sel:[0,0,1]
	v_cvt_pk_fp8_f32 v91, v92, v93 op_sel:[0,0,1]
	v_pk_mul_f32 v[92:93], v[108:109], v[186:187] op_sel_hi:[1,0]
	v_pk_mul_f32 v[94:95], v[106:107], v[186:187] op_sel_hi:[1,0]
	v_pk_mul_f32 v[88:89], v[92:93], v[88:89]
	v_pk_mul_f32 v[86:87], v[94:95], v[86:87]
	v_pk_mul_f32 v[92:93], v[112:113], v[186:187] op_sel_hi:[1,0]
	v_pk_mul_f32 v[94:95], v[110:111], v[186:187] op_sel_hi:[1,0]
	v_pk_mul_f32 v[80:81], v[92:93], v[80:81]
	v_pk_mul_f32 v[92:93], v[94:95], v[78:79]
	v_mov_b32_e32 v78, v147
	v_cvt_pk_fp8_f32 v78, v86, v87
	v_mov_b32_e32 v79, v147
	v_cvt_pk_fp8_f32 v79, v92, v93
	v_cvt_f32_i32_e32 v85, v85
	v_cvt_f32_i32_e32 v84, v84
	v_cvt_pk_fp8_f32 v79, v80, v81 op_sel:[0,0,1]
	v_mov_b32_e32 v80, v187
	v_cvt_pk_fp8_f32 v78, v88, v89 op_sel:[0,0,1]
	v_pk_mul_f32 v[86:87], v[120:121], v[80:81] op_sel_hi:[1,0]
	v_cvt_f32_i32_e32 v75, v75
	v_cvt_f32_i32_e32 v74, v74
	v_cvt_f32_i32_e32 v83, v83
	v_cvt_f32_i32_e32 v82, v82
	v_pk_mul_f32 v[84:85], v[86:87], v[84:85]
	v_pk_mul_f32 v[88:89], v[118:119], v[80:81] op_sel_hi:[1,0]
	v_pk_mul_f32 v[86:87], v[114:115], v[80:81] op_sel_hi:[1,0]
	v_cvt_f32_i32_e32 v77, v77
	v_cvt_f32_i32_e32 v76, v76
	v_pk_mul_f32 v[74:75], v[86:87], v[74:75]
	v_pk_mul_f32 v[82:83], v[88:89], v[82:83]
	v_mov_b32_e32 v92, v147
	v_mov_b32_e32 v93, v147
	v_cvt_pk_fp8_f32 v92, v74, v75
	v_cvt_pk_fp8_f32 v93, v82, v83
	v_pk_mul_f32 v[82:83], v[116:117], v[80:81] op_sel_hi:[1,0]
	v_cndmask_b32_e32 v122, v122, v123, vcc
	v_pk_mul_f32 v[74:75], v[82:83], v[76:77]
	v_cmp_eq_u32_e32 vcc, 1, v166
	v_cvt_pk_fp8_f32 v92, v74, v75 op_sel:[0,0,1]
	v_cndmask_b32_e64 v122, v122, v142, s[10:11]
	v_cvt_pk_fp8_f32 v93, v84, v85 op_sel:[0,0,1]
	v_cndmask_b32_e32 v74, v134, v135, vcc
	v_cmp_eq_u32_e64 s[10:11], 2, v166
	s_ashr_i32 s1, s0, 31
	v_cmp_eq_u32_e64 s[12:13], 3, v166
	v_cndmask_b32_e64 v74, v74, v123, s[10:11]
	s_lshl_b64 s[0:1], s[0:1], 18
	v_cndmask_b32_e64 v74, v74, v142, s[12:13]
	s_add_u32 s38, s36, s0
	v_ashrrev_i32_e32 v75, 31, v74
	s_addc_u32 s39, s37, s1
	v_lshlrev_b64 v[74:75], 7, v[74:75]
	v_cvt_f32_i32_e32 v71, v71
	v_cvt_f32_i32_e32 v70, v70
	v_lshl_add_u64 v[76:77], s[38:39], 0, v[74:75]
	v_lshl_add_u64 v[76:77], v[76:77], 0, s[20:21]
	v_lshl_add_u64 v[76:77], v[76:77], 0, v[160:161]
	v_pk_mul_f32 v[82:83], v[110:111], v[80:81] op_sel_hi:[1,0]
	v_permlane16_swap_b32_e32 v90, v92
	v_permlane16_swap_b32_e32 v91, v93
	v_lshl_add_u64 v[76:77], v[76:77], 0, v[164:165]
	v_pk_mul_f32 v[70:71], v[82:83], v[70:71]
	global_store_dwordx4 v[76:77], v[90:93], off
	v_pk_mul_f32 v[76:77], v[112:113], v[80:81] op_sel_hi:[1,0]
	v_mov_b32_e32 v81, v147
	v_cvt_f32_i32_e32 v73, v73
	v_cvt_f32_i32_e32 v72, v72
	v_cvt_pk_fp8_f32 v81, v70, v71
	v_cvt_f32_i32_e32 v59, v59
	v_cvt_f32_i32_e32 v58, v58
	v_cvt_f32_i32_e32 v61, v61
	v_cvt_f32_i32_e32 v60, v60
	v_pk_mul_f32 v[72:73], v[76:77], v[72:73]
	v_pk_mul_f32 v[76:77], v[106:107], v[80:81] op_sel_hi:[1,0]
	v_cvt_f32_i32_e32 v55, v55
	v_cvt_f32_i32_e32 v57, v57
	v_cvt_f32_i32_e32 v56, v56
	v_cvt_f32_i32_e32 v54, v54
	v_pk_mul_f32 v[58:59], v[76:77], v[58:59]
	v_cvt_f32_i32_e32 v51, v51
	v_cvt_f32_i32_e32 v53, v53
	v_cvt_f32_i32_e32 v52, v52
	v_cvt_f32_i32_e32 v50, v50
	v_pk_mul_f32 v[70:71], v[108:109], v[80:81] op_sel_hi:[1,0]
	v_mov_b32_e32 v80, v147
	v_cvt_pk_fp8_f32 v80, v58, v59
	v_pk_mul_f32 v[58:59], v[70:71], v[60:61]
	v_pk_mul_f32 v[60:61], v[116:117], v[184:185] op_sel_hi:[1,0]
	v_pk_mul_f32 v[70:71], v[114:115], v[184:185] op_sel_hi:[1,0]
	v_pk_mul_f32 v[56:57], v[60:61], v[56:57]
	v_pk_mul_f32 v[54:55], v[70:71], v[54:55]
	v_pk_mul_f32 v[60:61], v[120:121], v[184:185] op_sel_hi:[1,0]
	v_pk_mul_f32 v[70:71], v[118:119], v[184:185] op_sel_hi:[1,0]
	v_pk_mul_f32 v[52:53], v[60:61], v[52:53]
	v_pk_mul_f32 v[60:61], v[70:71], v[50:51]
	v_mov_b32_e32 v50, v147
	v_cvt_pk_fp8_f32 v50, v54, v55
	v_mov_b32_e32 v51, v147
	v_cvt_pk_fp8_f32 v51, v60, v61
	v_cvt_pk_fp8_f32 v50, v56, v57 op_sel:[0,0,1]
	v_cvt_f32_i32_e32 v55, v69
	v_cvt_f32_i32_e32 v54, v68
	v_cvt_pk_fp8_f32 v51, v52, v53 op_sel:[0,0,1]
	v_cvt_f32_i32_e32 v53, v67
	v_cvt_f32_i32_e32 v52, v66
	v_cvt_pk_fp8_f32 v80, v58, v59 op_sel:[0,0,1]
	s_add_u32 s0, s4, s0
	v_cvt_pk_fp8_f32 v81, v72, v73 op_sel:[0,0,1]
	s_addc_u32 s1, s5, s1
	v_pk_mul_f32 v[56:57], v[108:109], v[184:185] op_sel_hi:[1,0]
	v_lshl_add_u64 v[58:59], s[0:1], 0, v[74:75]
	v_pk_mul_f32 v[60:61], v[106:107], v[184:185] op_sel_hi:[1,0]
	v_pk_mul_f32 v[54:55], v[56:57], v[54:55]
	v_cvt_f32_i32_e32 v57, v63
	v_cvt_f32_i32_e32 v56, v62
	v_lshl_add_u64 v[58:59], v[58:59], 0, s[20:21]
	v_pk_mul_f32 v[52:53], v[60:61], v[52:53]
	v_cvt_f32_i32_e32 v61, v65
	v_cvt_f32_i32_e32 v60, v64
	v_lshl_add_u64 v[58:59], v[58:59], 0, v[160:161]
	v_permlane16_swap_b32_e32 v78, v80
	v_permlane16_swap_b32_e32 v79, v81
	v_lshl_add_u64 v[58:59], v[58:59], 0, v[164:165]
	v_pk_mul_f32 v[64:65], v[110:111], v[184:185] op_sel_hi:[1,0]
	global_store_dwordx4 v[58:59], v[78:81], off
	v_pk_mul_f32 v[62:63], v[112:113], v[184:185] op_sel_hi:[1,0]
	v_pk_mul_f32 v[56:57], v[64:65], v[56:57]
	v_mov_b32_e32 v59, v54
	v_mov_b32_e32 v54, v147
	v_pk_mul_f32 v[60:61], v[62:63], v[60:61]
	v_mov_b32_e32 v62, v55
	v_cvt_pk_fp8_f32 v54, v52, v53
	v_mov_b32_e32 v55, v147
	v_cvt_f32_i32_e32 v39, v39
	v_cvt_f32_i32_e32 v38, v38
	v_cvt_pk_fp8_f32 v55, v56, v57
	v_cvt_f32_i32_e32 v35, v35
	v_cvt_f32_i32_e32 v34, v34
	v_mov_b32_e32 v56, v185
	v_cvt_f32_i32_e32 v41, v41
	v_cvt_f32_i32_e32 v40, v40
	v_mov_b32_e32 v52, v60
	v_mov_b32_e32 v53, v61
	v_pk_mul_f32 v[60:61], v[118:119], v[56:57] op_sel_hi:[1,0]
	v_cvt_pk_fp8_f32 v55, v52, v53 op_sel:[0,0,1]
	v_pk_mul_f32 v[38:39], v[60:61], v[38:39]
	v_pk_mul_f32 v[60:61], v[114:115], v[56:57] op_sel_hi:[1,0]
	v_pk_mul_f32 v[52:53], v[120:121], v[56:57] op_sel_hi:[1,0]
	v_cvt_f32_i32_e32 v37, v37
	v_cvt_f32_i32_e32 v36, v36
	v_pk_mul_f32 v[34:35], v[60:61], v[34:35]
	v_pk_mul_f32 v[40:41], v[52:53], v[40:41]
	v_mov_b32_e32 v52, v147
	v_mov_b32_e32 v53, v147
	v_cvt_pk_fp8_f32 v52, v34, v35
	v_cvt_pk_fp8_f32 v53, v38, v39
	v_pk_mul_f32 v[38:39], v[116:117], v[56:57] op_sel_hi:[1,0]
	v_ashrrev_i32_e32 v58, 11, v143
	v_pk_mul_f32 v[34:35], v[38:39], v[36:37]
	v_cvt_pk_fp8_f32 v52, v34, v35 op_sel:[0,0,1]
	v_cvt_pk_fp8_f32 v53, v40, v41 op_sel:[0,0,1]
	v_cndmask_b32_e64 v34, v58, v127, s[14:15]
	v_ashrrev_i32_e32 v35, 31, v34
	v_lshlrev_b64 v[34:35], 18, v[34:35]
	v_ashrrev_i32_e32 v123, 31, v122
	v_lshl_add_u64 v[36:37], s[36:37], 0, v[34:35]
	v_lshlrev_b64 v[38:39], 7, v[122:123]
	v_lshl_add_u64 v[36:37], v[36:37], 0, v[38:39]
	v_lshl_add_u64 v[36:37], v[36:37], 0, s[20:21]
	v_cvt_f32_i32_e32 v41, v47
	v_cvt_f32_i32_e32 v40, v46
	v_lshl_add_u64 v[36:37], v[36:37], 0, v[160:161]
	v_permlane16_swap_b32_e32 v50, v52
	v_permlane16_swap_b32_e32 v51, v53
	v_lshl_add_u64 v[36:37], v[36:37], 0, v[164:165]
	global_store_dwordx4 v[36:37], v[50:53], off
	v_cvt_f32_i32_e32 v37, v49
	v_cvt_f32_i32_e32 v36, v48
	v_pk_mul_f32 v[48:49], v[110:111], v[56:57] op_sel_hi:[1,0]
	v_pk_mul_f32 v[46:47], v[112:113], v[56:57] op_sel_hi:[1,0]
	v_pk_mul_f32 v[40:41], v[48:49], v[40:41]
	v_mov_b32_e32 v57, v147
	v_cvt_pk_fp8_f32 v57, v40, v41
	v_cvt_f32_i32_e32 v43, v43
	v_cvt_f32_i32_e32 v42, v42
	v_pk_mul_f32 v[36:37], v[46:47], v[36:37]
	v_pk_mul_f32 v[46:47], v[106:107], v[56:57] op_sel_hi:[1,0]
	v_cvt_f32_i32_e32 v45, v45
	v_cvt_f32_i32_e32 v44, v44
	v_pk_mul_f32 v[42:43], v[46:47], v[42:43]
	v_pk_mul_f32 v[40:41], v[108:109], v[56:57] op_sel_hi:[1,0]
	v_mov_b32_e32 v56, v147
	v_cvt_pk_fp8_f32 v56, v42, v43
	v_pk_mul_f32 v[40:41], v[40:41], v[44:45]
	v_cvt_pk_fp8_f32 v54, v59, v62 op_sel:[0,0,1]
	v_cvt_pk_fp8_f32 v56, v40, v41 op_sel:[0,0,1]
	v_cvt_pk_fp8_f32 v57, v36, v37 op_sel:[0,0,1]
	v_lshl_add_u64 v[34:35], s[4:5], 0, v[34:35]
	v_lshl_add_u64 v[34:35], v[34:35], 0, v[38:39]
	v_lshl_add_u64 v[34:35], v[34:35], 0, s[20:21]
	v_lshl_add_u64 v[34:35], v[34:35], 0, v[160:161]
	v_permlane16_swap_b32_e32 v54, v56
	v_permlane16_swap_b32_e32 v55, v57
	v_lshl_add_u64 v[34:35], v[34:35], 0, v[164:165]
	global_store_dwordx4 v[34:35], v[54:57], off
	v_or_b32_e32 v34, 32, v124
	v_cvt_f32_i32_e32 v23, v23
	v_cvt_f32_i32_e32 v25, v25
	v_cvt_f32_i32_e32 v24, v24
	v_cvt_f32_i32_e32 v22, v22
	v_lshlrev_b32_e32 v35, s29, v34
	v_cvt_f32_i32_e32 v19, v19
	v_cvt_f32_i32_e32 v21, v21
	v_cvt_f32_i32_e32 v20, v20
	v_cvt_f32_i32_e32 v18, v18
	v_and_b32_e32 v35, 0x7fe, v35
	v_lshrrev_b32_e32 v34, s19, v34
	v_add_u32_e32 v38, v35, v34
	v_pk_mul_f32 v[34:35], v[116:117], v[182:183] op_sel_hi:[1,0]
	v_pk_mul_f32 v[36:37], v[114:115], v[182:183] op_sel_hi:[1,0]
	v_pk_mul_f32 v[24:25], v[34:35], v[24:25]
	v_pk_mul_f32 v[22:23], v[36:37], v[22:23]
	v_pk_mul_f32 v[34:35], v[120:121], v[182:183] op_sel_hi:[1,0]
	v_pk_mul_f32 v[36:37], v[118:119], v[182:183] op_sel_hi:[1,0]
	v_pk_mul_f32 v[20:21], v[34:35], v[20:21]
	v_pk_mul_f32 v[34:35], v[36:37], v[18:19]
	v_mov_b32_e32 v18, v147
	v_cvt_pk_fp8_f32 v18, v22, v23
	v_mov_b32_e32 v19, v147
	v_cvt_pk_fp8_f32 v19, v34, v35
	v_cvt_pk_fp8_f32 v18, v24, v25 op_sel:[0,0,1]
	v_cvt_f32_i32_e32 v23, v33
	v_cvt_f32_i32_e32 v22, v32
	v_cvt_pk_fp8_f32 v19, v20, v21 op_sel:[0,0,1]
	v_cvt_f32_i32_e32 v21, v31
	v_cvt_f32_i32_e32 v20, v30
	v_pk_mul_f32 v[24:25], v[108:109], v[182:183] op_sel_hi:[1,0]
	v_cvt_f32_i32_e32 v29, v29
	v_pk_mul_f32 v[22:23], v[24:25], v[22:23]
	v_cvt_f32_i32_e32 v25, v27
	v_cvt_f32_i32_e32 v28, v28
	v_cvt_f32_i32_e32 v24, v26
	v_pk_mul_f32 v[30:31], v[106:107], v[182:183] op_sel_hi:[1,0]
	v_pk_mul_f32 v[26:27], v[112:113], v[182:183] op_sel_hi:[1,0]
	v_pk_mul_f32 v[20:21], v[30:31], v[20:21]
	v_pk_mul_f32 v[30:31], v[110:111], v[182:183] op_sel_hi:[1,0]
	v_pk_mul_f32 v[26:27], v[26:27], v[28:29]
	v_pk_mul_f32 v[24:25], v[30:31], v[24:25]
	v_mov_b32_e32 v28, v22
	v_mov_b32_e32 v22, v147
	v_mov_b32_e32 v29, v23
	v_cvt_pk_fp8_f32 v22, v20, v21
	v_mov_b32_e32 v23, v147
	v_cvt_pk_fp8_f32 v23, v24, v25
	v_cvt_f32_i32_e32 v7, v7
	v_cvt_pk_fp8_f32 v23, v26, v27 op_sel:[0,0,1]
	v_or_b32_e32 v20, 48, v124
	v_lshlrev_b32_e32 v21, s29, v20
	v_cvt_f32_i32_e32 v6, v6
	v_and_b32_e32 v21, 0x7fe, v21
	v_lshrrev_b32_e32 v20, s19, v20
	v_cvt_f32_i32_e32 v3, v3
	v_cvt_f32_i32_e32 v2, v2
	v_add_u32_e32 v25, v21, v20
	v_mov_b32_e32 v24, v183
	v_cvt_f32_i32_e32 v9, v9
	v_cvt_f32_i32_e32 v8, v8
	v_pk_mul_f32 v[26:27], v[118:119], v[24:25] op_sel_hi:[1,0]
	v_pk_mul_f32 v[20:21], v[120:121], v[24:25] op_sel_hi:[1,0]
	v_pk_mul_f32 v[6:7], v[26:27], v[6:7]
	v_pk_mul_f32 v[26:27], v[114:115], v[24:25] op_sel_hi:[1,0]
	v_cvt_f32_i32_e32 v5, v5
	v_cvt_f32_i32_e32 v4, v4
	v_pk_mul_f32 v[2:3], v[26:27], v[2:3]
	v_pk_mul_f32 v[8:9], v[20:21], v[8:9]
	v_mov_b32_e32 v20, v147
	v_mov_b32_e32 v21, v147
	v_cvt_pk_fp8_f32 v20, v2, v3
	v_cvt_pk_fp8_f32 v21, v6, v7
	v_pk_mul_f32 v[6:7], v[116:117], v[24:25] op_sel_hi:[1,0]
	v_pk_mul_f32 v[2:3], v[6:7], v[4:5]
	v_cndmask_b32_e32 v6, v125, v126, vcc
	v_cndmask_b32_e64 v6, v6, v38, s[10:11]
	v_cvt_pk_fp8_f32 v20, v2, v3 op_sel:[0,0,1]
	v_ashrrev_i32_e32 v59, 31, v58
	v_cndmask_b32_e64 v6, v6, v25, s[12:13]
	v_cvt_pk_fp8_f32 v21, v8, v9 op_sel:[0,0,1]
	v_lshlrev_b64 v[2:3], 18, v[58:59]
	v_ashrrev_i32_e32 v7, 31, v6
	v_lshl_add_u64 v[4:5], s[36:37], 0, v[2:3]
	v_lshlrev_b64 v[6:7], 7, v[6:7]
	v_lshl_add_u64 v[4:5], v[4:5], 0, v[6:7]
	v_lshl_add_u64 v[4:5], v[4:5], 0, s[20:21]
	v_cvt_f32_i32_e32 v9, v15
	v_cvt_f32_i32_e32 v8, v14
	v_lshl_add_u64 v[4:5], v[4:5], 0, v[160:161]
	v_permlane16_swap_b32_e32 v18, v20
	v_permlane16_swap_b32_e32 v19, v21
	v_lshl_add_u64 v[4:5], v[4:5], 0, v[164:165]
	global_store_dwordx4 v[4:5], v[18:21], off
	v_cvt_f32_i32_e32 v5, v17
	v_cvt_f32_i32_e32 v4, v16
	v_pk_mul_f32 v[16:17], v[110:111], v[24:25] op_sel_hi:[1,0]
	v_pk_mul_f32 v[14:15], v[112:113], v[24:25] op_sel_hi:[1,0]
	v_pk_mul_f32 v[8:9], v[16:17], v[8:9]
	v_mov_b32_e32 v25, v147
	v_cvt_pk_fp8_f32 v25, v8, v9
	v_cvt_f32_i32_e32 v11, v11
	v_cvt_f32_i32_e32 v10, v10
	v_pk_mul_f32 v[4:5], v[14:15], v[4:5]
	v_pk_mul_f32 v[14:15], v[106:107], v[24:25] op_sel_hi:[1,0]
	v_cvt_f32_i32_e32 v13, v13
	v_cvt_f32_i32_e32 v12, v12
	v_pk_mul_f32 v[10:11], v[14:15], v[10:11]
	v_pk_mul_f32 v[8:9], v[108:109], v[24:25] op_sel_hi:[1,0]
	v_mov_b32_e32 v24, v147
	v_cvt_pk_fp8_f32 v24, v10, v11
	v_pk_mul_f32 v[8:9], v[8:9], v[12:13]
	v_cvt_pk_fp8_f32 v22, v28, v29 op_sel:[0,0,1]
	v_cvt_pk_fp8_f32 v24, v8, v9 op_sel:[0,0,1]
	v_cvt_pk_fp8_f32 v25, v4, v5 op_sel:[0,0,1]
	v_lshl_add_u64 v[2:3], s[4:5], 0, v[2:3]
	v_lshl_add_u64 v[2:3], v[2:3], 0, v[6:7]
	v_lshl_add_u64 v[2:3], v[2:3], 0, s[20:21]
	v_lshl_add_u64 v[2:3], v[2:3], 0, v[160:161]
	v_permlane16_swap_b32_e32 v22, v24
	v_permlane16_swap_b32_e32 v23, v25
	v_lshl_add_u64 v[2:3], v[2:3], 0, v[164:165]
	global_store_dwordx4 v[2:3], v[22:25], off
	s_and_b64 vcc, exec, s[8:9]
	s_mov_b64 s[0:1], -1
	s_cbranch_vccnz .LBB0_234
